# router top-6: 16 of the 24 DPP exchange stages evaluate the better-lane predicate with compares and scalar mask ops instead of nested exec-masked branches
# baseline (speedup 1.0000x reference)
; __device__ __forceinline__ void ph_ln_router(const Frame& F, int l, bool dry = false) {
;     ...
;     for (int tile = TILE0 + F.wg; tile < NTILE; tile += F.G) {
;         const int row = tile * 16 + tk; const int s = slot_of_row(tile * 16);
;         const float* ab = (const float*)(F.ws + OFF_AB) + (size_t)(l * 5 + s) * 2048;
;         f32x4 v[4][2];
; #pragma unroll
;         for (int ks = 0; ks < 4; ++ks) { v[ks][0] = vn[ks][0]; v[ks][1] = vn[ks][1]; }
;         if (tile + F.G < NTILE) { const float* xr = F.X + (size_t)((tile + F.G) * 16 + tk) * DM + F.wave * 128 + g * 8;
; #pragma unroll
;             for (int ks = 0; ks < 4; ++ks) { vn[ks][0] = *(const f32x4*)(xr + ks * 32); vn[ks][1] = *(const f32x4*)(xr + ks * 32 + 4); } }
;         float sum = 0.f, sq = 0.f;
; #pragma unroll
;         for (int ks = 0; ks < 4; ++ks)
; #pragma unroll
;             for (int hh = 0; hh < 2; ++hh) { const f32x4 a = v[ks][hh]; sum += (a[0] + a[1]) + (a[2] + a[3]); sq += (a[0] * a[0] + a[1] * a[1]) + (a[2] * a[2] + a[3] * a[3]); }
;         sum = rows_sum(sum); sq = rows_sum(sq);
;         if (g == 0) *(LAS f32x2*)(part + (F.wave * 16 + tk) * 2) = (f32x2){sum, sq};
;         lds_barrier();
;         float ts = 0.f, tq = 0.f;
; #pragma unroll
;         for (int w = 0; w < 8; ++w) { const f32x2 p = *(const LAS f32x2*)(part + (w * 16 + tk) * 2); ts += p.x; tq += p.y; }
;         const float mean = ts * (1.0f / 1024.0f), var = fmaxf(tq * (1.0f / 1024.0f) - mean * mean, 0.f), rstd = rsqrtf(var + 1e-5f);
;         if (F.wave == 0 && g == 0) *(f32x2*)(stats + (size_t)row * 2) = (f32x2){mean, rstd};
;         f32x4 acc[4];
; #pragma unroll
;         for (int et = 0; et < 4; ++et) acc[et] = (f32x4){0.f, 0.f, 0.f, 0.f};
; #pragma unroll
;         for (int ks = 0; ks < 4; ++ks) { const int k = F.wave * 128 + ks * 32 + g * 8;
;             const f32x4 a10 = *(const f32x4*)(ab + k), a11 = *(const f32x4*)(ab + k + 4), b10 = *(const f32x4*)(ab + 1024 + k), b11 = *(const f32x4*)(ab + 1024 + k + 4);
;             const f32x4 h0 = (v[ks][0] - mean) * rstd * a10 + b10, h1 = (v[ks][1] - mean) * rstd * a11 + b11;
;             u32x4 w; w.x = cvt_pk_bf16(h0[0], h0[1]); w.y = cvt_pk_bf16(h0[2], h0[3]); w.z = cvt_pk_bf16(h1[0], h1[1]); w.w = cvt_pk_bf16(h1[2], h1[3]);
;             *(u32x4*)(F.HB + (size_t)row * DM + k) = w;
;             bf16x8 af; __builtin_memcpy(&af, &w, 16);
; #pragma unroll
.LBB0_1320:
	s_or_b64 exec, exec, s[8:9]
	v_readlane_b32 s8, v254, 0
	s_add_i32 s8, s8, s13
	s_lshr_b32 s8, s8, 13
	s_cmp_gt_i32 s2, 63
	s_cselect_b32 s2, s8, 4
	v_readlane_b32 s8, v255, 2
	s_mul_i32 s8, s8, 5
	v_readlane_b32 s9, v255, 3
	s_add_i32 s64, s2, s8
	s_lshl_b64 s[8:9], s[64:65], 13
	v_readlane_b32 s2, v252, 18
	s_add_u32 s54, s2, s8
	v_readlane_b32 s2, v252, 19
	s_addc_u32 s55, s2, s9
	s_add_u32 s8, s54, 0x1000
	s_addc_u32 s9, s55, 0
	v_lshlrev_b64 v[190:191], 2, v[136:137]
	v_lshl_add_u64 v[170:171], s[54:55], 0, v[190:191]
	v_lshl_add_u64 v[194:195], s[8:9], 0, v[190:191]
	global_load_dwordx4 v[166:169], v[170:171], off offset:16
	s_nop 0
	global_load_dwordx4 v[170:173], v[170:171], off
	s_nop 0
	global_load_dwordx4 v[190:193], v[194:195], off offset:16
	s_nop 0
	global_load_dwordx4 v[194:197], v[194:195], off
	v_lshlrev_b64 v[246:247], 2, v[138:139]
	v_lshl_add_u64 v[248:249], s[8:9], 0, v[246:247]
	v_lshl_add_u64 v[246:247], s[54:55], 0, v[246:247]
	global_load_dwordx4 v[210:213], v[246:247], off offset:16
	global_load_dwordx4 v[198:201], v[246:247], off
	global_load_dwordx4 v[202:205], v[248:249], off offset:16
	global_load_dwordx4 v[206:209], v[248:249], off
	v_lshlrev_b64 v[246:247], 2, v[140:141]
	v_lshl_add_u64 v[248:249], s[8:9], 0, v[246:247]
	v_lshl_add_u64 v[246:247], s[54:55], 0, v[246:247]
	global_load_dwordx4 v[214:217], v[246:247], off offset:16
	global_load_dwordx4 v[218:221], v[246:247], off
	global_load_dwordx4 v[222:225], v[248:249], off offset:16
	global_load_dwordx4 v[226:229], v[248:249], off
	v_lshlrev_b64 v[246:247], 2, v[142:143]
	v_lshl_add_u64 v[248:249], s[8:9], 0, v[246:247]
	v_lshl_add_u64 v[246:247], s[54:55], 0, v[246:247]
	global_load_dwordx4 v[230:233], v[246:247], off offset:16
	global_load_dwordx4 v[234:237], v[246:247], off
	global_load_dwordx4 v[238:241], v[248:249], off offset:16
	global_load_dwordx4 v[242:245], v[248:249], off
	v_sub_f32_e32 v129, v129, v148
	v_sub_f32_e32 v128, v128, v148
	v_sub_f32_e32 v125, v125, v148
	v_sub_f32_e32 v124, v124, v148
	v_sub_f32_e32 v131, v131, v148
	v_sub_f32_e32 v130, v130, v148
	v_pk_mul_f32 v[128:129], v[128:129], v[150:151] op_sel_hi:[1,0]
	v_sub_f32_e32 v127, v127, v148
	v_sub_f32_e32 v126, v126, v148
	v_pk_mul_f32 v[124:125], v[124:125], v[150:151] op_sel_hi:[1,0]
	v_lshlrev_b64 v[152:153], 11, v[152:153]
	v_pk_mul_f32 v[130:131], v[130:131], v[150:151] op_sel_hi:[1,0]
	v_pk_mul_f32 v[126:127], v[126:127], v[150:151] op_sel_hi:[1,0]
	v_sub_f32_e32 v121, v121, v148
	v_sub_f32_e32 v120, v120, v148
	v_sub_f32_e32 v119, v119, v148
	v_sub_f32_e32 v118, v118, v148
	v_sub_f32_e32 v117, v117, v148
	v_sub_f32_e32 v116, v116, v148
	v_sub_f32_e32 v123, v123, v148
	v_sub_f32_e32 v122, v122, v148
	v_pk_mul_f32 v[120:121], v[120:121], v[150:151] op_sel_hi:[1,0]
	v_pk_mul_f32 v[116:117], v[116:117], v[150:151] op_sel_hi:[1,0]
	v_pk_mul_f32 v[118:119], v[118:119], v[150:151] op_sel_hi:[1,0]
	v_pk_mul_f32 v[122:123], v[122:123], v[150:151] op_sel_hi:[1,0]
	v_sub_f32_e32 v113, v113, v148
	v_sub_f32_e32 v112, v112, v148
	v_pk_mul_f32 v[112:113], v[112:113], v[150:151] op_sel_hi:[1,0]
	v_sub_f32_e32 v111, v111, v148
	v_sub_f32_e32 v110, v110, v148
	v_sub_f32_e32 v109, v109, v148
	v_sub_f32_e32 v108, v108, v148
	v_sub_f32_e32 v115, v115, v148
	v_sub_f32_e32 v114, v114, v148
	v_pk_mul_f32 v[108:109], v[108:109], v[150:151] op_sel_hi:[1,0]
	v_pk_mul_f32 v[110:111], v[110:111], v[150:151] op_sel_hi:[1,0]
	v_pk_mul_f32 v[114:115], v[114:115], v[150:151] op_sel_hi:[1,0]
	v_sub_f32_e32 v105, v105, v148
	v_sub_f32_e32 v104, v104, v148
	v_sub_f32_e32 v107, v107, v148
	v_sub_f32_e32 v106, v106, v148
	v_pk_mul_f32 v[104:105], v[104:105], v[150:151] op_sel_hi:[1,0]
	v_sub_f32_e32 v103, v103, v148
	v_sub_f32_e32 v102, v102, v148
	v_sub_f32_e32 v101, v101, v148
	v_sub_f32_e32 v100, v100, v148
	v_pk_mul_f32 v[106:107], v[106:107], v[150:151] op_sel_hi:[1,0]
	v_pk_mul_f32 v[100:101], v[100:101], v[150:151] op_sel_hi:[1,0]
	v_pk_mul_f32 v[102:103], v[102:103], v[150:151] op_sel_hi:[1,0]
	s_mov_b32 s2, 0xf149f2ca
	s_mov_b64 s[30:31], -1
	s_waitcnt vmcnt(13)
	v_pk_fma_f32 v[124:125], v[124:125], v[166:167], v[190:191]
	s_waitcnt vmcnt(12)
	v_pk_fma_f32 v[128:129], v[128:129], v[170:171], v[194:195]
	v_pk_fma_f32 v[130:131], v[130:131], v[172:173], v[196:197]
	v_pk_fma_f32 v[168:169], v[126:127], v[168:169], v[192:193]
	v_cvt_pk_bf16_f32 v126, v128, v129
	v_cvt_pk_bf16_f32 v127, v130, v131
	v_cvt_pk_bf16_f32 v128, v124, v125
	v_lshl_add_u64 v[124:125], s[76:77], 0, v[152:153]
	v_lshl_add_u64 v[130:131], v[136:137], 1, v[124:125]
	v_cvt_pk_bf16_f32 v129, v168, v169
	global_store_dwordx4 v[130:131], v[126:129], off
	v_mfma_f32_16x16x32_bf16 v[166:169], v[126:129], v[12:15], 0
	s_waitcnt vmcnt(10)
	v_pk_fma_f32 v[130:131], v[118:119], v[212:213], v[204:205]
	v_mfma_f32_16x16x32_bf16 v[170:173], v[126:129], v[20:23], 0
	s_waitcnt vmcnt(9)
	v_pk_fma_f32 v[120:121], v[120:121], v[198:199], v[206:207]
	v_pk_fma_f32 v[118:119], v[116:117], v[210:211], v[202:203]
	v_pk_fma_f32 v[122:123], v[122:123], v[200:201], v[208:209]
	v_mfma_f32_16x16x32_bf16 v[190:193], v[126:129], v[36:39], 0
	v_cvt_pk_bf16_f32 v116, v120, v121
	v_cvt_pk_bf16_f32 v117, v122, v123
	v_cvt_pk_bf16_f32 v118, v118, v119
	v_mfma_f32_16x16x32_bf16 v[126:129], v[126:129], v[52:55], 0
	v_cvt_pk_bf16_f32 v119, v130, v131
	v_lshl_add_u64 v[120:121], v[138:139], 1, v[124:125]
	global_store_dwordx4 v[120:121], v[116:119], off
	v_mfma_f32_16x16x32_bf16 v[120:123], v[116:119], v[4:7], v[166:169]
	v_mfma_f32_16x16x32_bf16 v[166:169], v[116:119], v[24:27], v[170:173]
	v_mfma_f32_16x16x32_bf16 v[170:173], v[116:119], v[40:43], v[190:193]
	v_mfma_f32_16x16x32_bf16 v[116:119], v[116:119], v[56:59], v[126:129]
	s_nop 2
	s_mov_b64 s[8:9], -1
	s_waitcnt vmcnt(7)
; __device__ __forceinline__ void lds_barrier() { asm volatile("s_waitcnt lgkmcnt(0)\n\ts_barrier" ::: "memory"); }
; __device__ __forceinline__ float sigmoidf_(float x) { return __builtin_amdgcn_rcpf(1.0f + __expf(-x)); }
; template <int CTRL> __device__ __forceinline__ void topk_step(float& bk, int& be, float& bs) {
;     const float ok = dppf<CTRL>(bk, bk), os = dppf<CTRL>(bs, bs); const int oe = __builtin_amdgcn_update_dpp(be, be, CTRL, 0xf, 0xf, false); topk_better(bk, be, bs, ok, oe, os); }
; __device__ __forceinline__ void ph_ln_router(const Frame& F, int l, bool dry = false) {
;     ...
; #pragma unroll
;         for (int et = 0; et < 4; ++et)
; #pragma unroll
;             for (int i = 0; i < 4; ++i) LP[(F.wave * 16 + 4 * g + i) * 64 + et * 16 + tk] = acc[et][i];
;         lds_barrier();
;         {
;             const int t = 2 * F.wave + (g & 1), r2 = tile * 16 + t;
;             float sc[4], key[4];
; #pragma unroll
;             for (int q = 0; q < 4; ++q) { float lgt = 0.f;
; #pragma unroll
;                 for (int w = 0; w < 8; ++w) lgt += LP[(w * 16 + t) * 64 + tk + 16 * q];
;                 sc[q] = sigmoidf_(lgt); key[q] = sc[q] + rb[q]; }
;             unsigned taken = 0u; int se[6]; float ss[6]; float tot = 0.f;
; #pragma unroll
;             for (int sel = 0; sel < 6; ++sel) {
;                 float bk = -1e30f, bs = 0.f; int be = 0;
; #pragma unroll
;                 for (int q = 0; q < 4; ++q) if (!((taken >> q) & 1u) && key[q] > bk) { bk = key[q]; be = tk + 16 * q; bs = sc[q]; }
;                 topk_step<0xB1>(bk, be, bs); topk_step<0x4E>(bk, be, bs); topk_step<0x141>(bk, be, bs); topk_step<0x140>(bk, be, bs);
	v_pk_fma_f32 v[128:129], v[110:111], v[216:217], v[224:225]
	s_waitcnt vmcnt(6)
	v_pk_fma_f32 v[112:113], v[112:113], v[218:219], v[226:227]
	v_pk_fma_f32 v[110:111], v[108:109], v[214:215], v[222:223]
	v_cvt_pk_bf16_f32 v108, v112, v113
	v_lshl_add_u64 v[112:113], v[140:141], 1, v[124:125]
	v_pk_fma_f32 v[114:115], v[114:115], v[220:221], v[228:229]
	s_nop 0
	v_cvt_pk_bf16_f32 v109, v114, v115
	v_cvt_pk_bf16_f32 v110, v110, v111
	v_cvt_pk_bf16_f32 v111, v128, v129
	global_store_dwordx4 v[112:113], v[108:111], off
	v_mfma_f32_16x16x32_bf16 v[112:115], v[108:111], v[8:11], v[120:123]
	v_mfma_f32_16x16x32_bf16 v[120:123], v[108:111], v[28:31], v[166:169]
	v_mfma_f32_16x16x32_bf16 v[126:129], v[108:111], v[44:47], v[170:173]
	v_mfma_f32_16x16x32_bf16 v[108:111], v[108:111], v[60:63], v[116:119]
	s_nop 2
	s_waitcnt vmcnt(4)
	v_pk_fma_f32 v[118:119], v[102:103], v[232:233], v[240:241]
	s_waitcnt vmcnt(3)
	v_pk_fma_f32 v[104:105], v[104:105], v[234:235], v[242:243]
	v_pk_fma_f32 v[106:107], v[106:107], v[236:237], v[244:245]
	v_pk_fma_f32 v[102:103], v[100:101], v[230:231], v[238:239]
	v_cvt_pk_bf16_f32 v100, v104, v105
	v_lshl_add_u64 v[104:105], v[142:143], 1, v[124:125]
	v_cvt_pk_bf16_f32 v101, v106, v107
	v_cvt_pk_bf16_f32 v102, v102, v103
	v_cvt_pk_bf16_f32 v103, v118, v119
	global_store_dwordx4 v[104:105], v[100:103], off
	v_mfma_f32_16x16x32_bf16 v[104:107], v[100:103], v[16:19], v[112:115]
	v_add_u32_e32 v124, 0x8000, v164
	v_mfma_f32_16x16x32_bf16 v[112:115], v[100:103], v[32:35], v[120:123]
	v_mfma_f32_16x16x32_bf16 v[116:119], v[100:103], v[48:51], v[126:129]
	s_nop 1
	v_add_u32_e32 v120, 0x4000, v164
	v_add_u32_e32 v121, 0x5000, v164
	v_add_u32_e32 v122, 0x6000, v164
	v_mfma_f32_16x16x32_bf16 v[100:103], v[100:103], v[64:67], v[108:111]
	v_add_u32_e32 v123, 0x7000, v164
	s_nop 1
	v_add_u32_e32 v108, 0x1000, v163
	ds_write2_b32 v108, v104, v112 offset1:16
	ds_write2_b32 v108, v105, v113 offset0:64 offset1:80
	ds_write2_b32 v108, v106, v114 offset0:128 offset1:144
	ds_write2_b32 v108, v107, v115 offset0:192 offset1:208
	ds_write2_b32 v108, v116, v100 offset0:32 offset1:48
	ds_write2_b32 v108, v117, v101 offset0:96 offset1:112
	ds_write2_b32 v108, v118, v102 offset0:160 offset1:176
	ds_write2_b32 v108, v119, v103 offset0:224 offset1:240
	s_waitcnt lgkmcnt(0)
	s_barrier
	v_add_u32_e32 v118, 0x1000, v164
	ds_read2_b32 v[102:103], v118 offset1:16
	v_add_u32_e32 v119, 0x2000, v164
	ds_read2_b32 v[104:105], v119 offset1:16
	ds_read2_b32 v[108:109], v120 offset1:16
	ds_read2_b32 v[110:111], v121 offset1:16
	s_waitcnt lgkmcnt(3)
	v_add_f32_e32 v100, 0, v102
	ds_read2_b32 v[112:113], v122 offset1:16
	s_waitcnt lgkmcnt(3)
	v_add_f32_e32 v100, v100, v104
	v_add_u32_e32 v104, 0x3000, v164
	ds_read2_b32 v[106:107], v104 offset1:16
	v_add_f32_e32 v102, 0, v103
	ds_read2_b32 v[114:115], v123 offset1:16
	v_add_f32_e32 v102, v102, v105
	ds_read2_b32 v[116:117], v124 offset1:16
	s_waitcnt lgkmcnt(2)
	v_add_f32_e32 v100, v100, v106
	v_add_f32_e32 v102, v102, v107
	ds_read2_b32 v[106:107], v118 offset0:32 offset1:48
	v_add_f32_e32 v100, v100, v108
	v_add_f32_e32 v102, v102, v109
	ds_read2_b32 v[108:109], v119 offset0:32 offset1:48
	v_add_f32_e32 v100, v100, v110
	v_add_f32_e32 v102, v102, v111
	ds_read2_b32 v[110:111], v104 offset0:32 offset1:48
	v_add_f32_e32 v100, v100, v112
	v_add_f32_e32 v102, v102, v113
	ds_read2_b32 v[112:113], v120 offset0:32 offset1:48
	s_waitcnt lgkmcnt(5)
	v_add_f32_e32 v100, v100, v114
	v_add_f32_e32 v102, v102, v115
	ds_read2_b32 v[114:115], v121 offset0:32 offset1:48
	s_waitcnt lgkmcnt(5)
	v_add_f32_e32 v100, v100, v116
	v_add_f32_e32 v102, v102, v117
	s_waitcnt lgkmcnt(4)
	v_add_f32_e32 v105, 0, v106
	ds_read2_b32 v[116:117], v122 offset0:32 offset1:48
	s_waitcnt lgkmcnt(4)
	v_add_f32_e32 v105, v105, v108
	ds_read2_b32 v[118:119], v123 offset0:32 offset1:48
	s_waitcnt lgkmcnt(4)
	v_add_f32_e32 v104, v105, v110
	ds_read2_b32 v[120:121], v124 offset0:32 offset1:48
	v_add_f32_e32 v106, 0, v107
	s_waitcnt lgkmcnt(4)
	v_add_f32_e32 v104, v104, v112
	v_add_f32_e32 v106, v106, v109
	v_mul_f32_e32 v100, 0xbfb8aa3b, v100
	s_waitcnt lgkmcnt(3)
	v_add_f32_e32 v104, v104, v114
	v_add_f32_e32 v106, v106, v111
	v_exp_f32_e32 v100, v100
	s_waitcnt lgkmcnt(2)
	v_add_f32_e32 v104, v104, v116
	v_add_f32_e32 v106, v106, v113
	v_mul_f32_e32 v102, 0xbfb8aa3b, v102
	s_waitcnt lgkmcnt(1)
	v_add_f32_e32 v104, v104, v118
	v_add_f32_e32 v106, v106, v115
	v_exp_f32_e32 v102, v102
	s_waitcnt lgkmcnt(0)
	v_add_f32_e32 v104, v104, v120
	v_add_f32_e32 v106, v106, v117
	v_mul_f32_e32 v104, 0xbfb8aa3b, v104
	v_add_f32_e32 v106, v106, v119
	v_add_f32_e32 v100, 1.0, v100
	v_exp_f32_e32 v104, v104
	v_add_f32_e32 v106, v106, v121
	v_rcp_f32_e32 v100, v100
	v_mul_f32_e32 v106, 0xbfb8aa3b, v106
	v_add_f32_e32 v102, 1.0, v102
	v_exp_f32_e32 v106, v106
	v_rcp_f32_e32 v102, v102
	v_add_f32_e32 v104, 1.0, v104
	v_add_f32_e32 v101, v133, v100
	v_rcp_f32_e32 v104, v104
	v_add_f32_e32 v106, 1.0, v106
	v_cmp_lt_f32_e32 vcc, s2, v101
	v_add_f32_e32 v103, v145, v102
	v_rcp_f32_e32 v106, v106
	v_cndmask_b32_e32 v108, v188, v101, vcc
	v_cmp_gt_f32_e64 s[54:55], v103, v108
	v_add_f32_e32 v105, v154, v104
	v_cndmask_b32_e32 v109, 0, v100, vcc
	v_cndmask_b32_e32 v110, 0, v1, vcc
	v_cndmask_b32_e64 v108, v108, v103, s[54:55]
	v_cndmask_b32_e64 v109, v109, v102, s[54:55]
	v_cndmask_b32_e64 v110, v110, v156, s[54:55]
	v_cmp_gt_f32_e64 s[54:55], v105, v108
	v_add_f32_e32 v107, v155, v106
	s_nop 0
	v_cndmask_b32_e64 v108, v108, v105, s[54:55]
	v_cndmask_b32_e64 v111, v109, v104, s[54:55]
	v_cndmask_b32_e64 v110, v110, v157, s[54:55]
	v_cmp_gt_f32_e64 s[54:55], v107, v108
	s_nop 1
	v_cndmask_b32_e64 v109, v108, v107, s[54:55]
	v_cndmask_b32_e64 v108, v111, v106, s[54:55]
	v_cndmask_b32_e64 v110, v110, v158, s[54:55]
	v_mov_b32_e32 v111, v109
	v_mov_b32_e32 v112, v108
	v_mov_b32_e32 v113, v110
	v_mov_b32_dpp v111, v111 quad_perm:[1,0,3,2] row_mask:0xf bank_mask:0xf
	v_mov_b32_dpp v112, v112 quad_perm:[1,0,3,2] row_mask:0xf bank_mask:0xf
	v_mov_b32_dpp v113, v113 quad_perm:[1,0,3,2] row_mask:0xf bank_mask:0xf
	v_cmp_gt_f32_e64 s[30:31], v111, v109
	v_cmp_eq_f32_e64 s[24:25], v111, v109
	v_cmp_lt_i32_e64 s[56:57], v113, v110
	s_and_b64 s[24:25], s[24:25], s[56:57]
	s_or_b64 s[30:31], s[30:31], s[24:25]
; template <int CTRL> __device__ __forceinline__ void topk_step(float& bk, int& be, float& bs) {
;     const float ok = dppf<CTRL>(bk, bk), os = dppf<CTRL>(bs, bs); const int oe = __builtin_amdgcn_update_dpp(be, be, CTRL, 0xf, 0xf, false); topk_better(bk, be, bs, ok, oe, os); }
; __device__ __forceinline__ void ph_ln_router(const Frame& F, int l, bool dry = false) {
;     ...
;             for (int sel = 0; sel < 6; ++sel) {
;                 float bk = -1e30f, bs = 0.f; int be = 0;
; #pragma unroll
;                 for (int q = 0; q < 4; ++q) if (!((taken >> q) & 1u) && key[q] > bk) { bk = key[q]; be = tk + 16 * q; bs = sc[q]; }
;                 topk_step<0xB1>(bk, be, bs); topk_step<0x4E>(bk, be, bs); topk_step<0x141>(bk, be, bs); topk_step<0x140>(bk, be, bs);
;                 if ((be & 15) == tk) taken |= 1u << (be >> 4);
;                 se[sel] = be; ss[sel] = bs; tot += bs;
.LBB0_1324:
	v_cndmask_b32_e64 v109, v109, v111, s[30:31]
	v_cndmask_b32_e64 v110, v110, v113, s[30:31]
	v_cndmask_b32_e64 v111, v108, v112, s[30:31]
	v_mov_b32_e32 v108, v109
	v_mov_b32_e32 v112, v111
	v_mov_b32_e32 v113, v110
	v_mov_b32_dpp v108, v108 quad_perm:[2,3,0,1] row_mask:0xf bank_mask:0xf
	v_mov_b32_dpp v112, v112 quad_perm:[2,3,0,1] row_mask:0xf bank_mask:0xf
	v_mov_b32_dpp v113, v113 quad_perm:[2,3,0,1] row_mask:0xf bank_mask:0xf
	v_cmp_gt_f32_e64 s[8:9], v108, v109
	v_cmp_eq_f32_e64 s[24:25], v108, v109
	v_cmp_lt_i32_e64 s[30:31], v113, v110
	s_and_b64 s[24:25], s[24:25], s[30:31]
	s_or_b64 s[8:9], s[8:9], s[24:25]
.LBB0_1328:
	v_cndmask_b32_e64 v108, v109, v108, s[8:9]
	v_cndmask_b32_e64 v109, v110, v113, s[8:9]
	v_cndmask_b32_e64 v110, v111, v112, s[8:9]
	v_mov_b32_e32 v111, v108
	v_mov_b32_e32 v112, v110
	v_mov_b32_e32 v113, v109
	v_mov_b32_dpp v111, v111 row_half_mirror row_mask:0xf bank_mask:0xf
	v_mov_b32_dpp v112, v112 row_half_mirror row_mask:0xf bank_mask:0xf
	v_mov_b32_dpp v113, v113 row_half_mirror row_mask:0xf bank_mask:0xf
	v_cmp_nlt_f32_e64 s[54:55], v108, v111
	s_mov_b64 s[8:9], -1
	s_mov_b64 s[30:31], -1
	s_and_saveexec_b64 s[24:25], s[54:55]
	s_cbranch_execz .LBB0_1332
	v_cmp_eq_f32_e64 s[54:55], v108, v111
	s_mov_b64 s[30:31], 0
	s_and_saveexec_b64 s[56:57], s[54:55]
	v_cmp_lt_i32_e64 s[54:55], v113, v109
	s_and_b64 s[30:31], s[54:55], exec
	s_or_b64 exec, exec, s[56:57]
	s_orn2_b64 s[30:31], s[30:31], exec
.LBB0_1332:
	s_or_b64 exec, exec, s[24:25]
	v_cndmask_b32_e64 v114, v108, v111, s[30:31]
	v_cndmask_b32_e64 v111, v109, v113, s[30:31]
	v_cndmask_b32_e64 v108, v110, v112, s[30:31]
	v_mov_b32_e32 v112, v114
	v_mov_b32_e32 v109, v108
	v_mov_b32_e32 v110, v111
	v_mov_b32_dpp v112, v112 row_mirror row_mask:0xf bank_mask:0xf
	v_mov_b32_dpp v109, v109 row_mirror row_mask:0xf bank_mask:0xf
	v_mov_b32_dpp v110, v110 row_mirror row_mask:0xf bank_mask:0xf
	v_cmp_gt_f32_e64 s[8:9], v112, v114
	v_cmp_eq_f32_e64 s[24:25], v112, v114
	v_cmp_lt_i32_e64 s[30:31], v110, v111
	s_and_b64 s[24:25], s[24:25], s[30:31]
	s_or_b64 s[8:9], s[8:9], s[24:25]
.LBB0_1336:
	v_cndmask_b32_e64 v110, v111, v110, s[8:9]
	v_and_b32_e32 v111, 15, v110
	v_ashrrev_i32_e32 v112, 4, v110
	v_lshlrev_b32_e64 v112, v112, 1
	v_cmp_eq_u32_e64 s[54:55], v111, v1
	s_mov_b64 s[24:25], -1
	s_mov_b64 s[56:57], -1
	v_cndmask_b32_e64 v116, 0, v112, s[54:55]
	v_and_b32_e32 v111, 1, v116
	v_cmp_eq_u32_e64 s[54:55], 0, v111
	s_and_b64 s[54:55], vcc, s[54:55]
	v_and_b32_e32 v114, 2, v116
	v_cndmask_b32_e64 v111, v188, v101, s[54:55]
	v_cndmask_b32_e64 v112, 0, v100, s[54:55]
	v_cndmask_b32_e64 v113, 0, v1, s[54:55]
	v_cmp_eq_u32_e64 s[54:55], 0, v114
	v_cmp_gt_f32_e64 s[58:59], v103, v111
	s_and_b64 s[54:55], s[54:55], s[58:59]
	v_cndmask_b32_e64 v111, v111, v103, s[54:55]
	v_and_b32_e32 v114, 4, v116
	v_cndmask_b32_e64 v112, v112, v102, s[54:55]
	v_cndmask_b32_e64 v113, v113, v156, s[54:55]
	v_cmp_eq_u32_e64 s[54:55], 0, v114
	v_cmp_gt_f32_e64 s[58:59], v105, v111
	s_and_b64 s[54:55], s[54:55], s[58:59]
	v_cndmask_b32_e64 v111, v111, v105, s[54:55]
	v_cndmask_b32_e64 v114, v112, v104, s[54:55]
	v_and_b32_e32 v112, 8, v116
	v_cndmask_b32_e64 v113, v113, v157, s[54:55]
	v_cmp_eq_u32_e64 s[54:55], 0, v112
	v_cmp_gt_f32_e64 s[58:59], v107, v111
	s_and_b64 s[54:55], s[54:55], s[58:59]
	v_cndmask_b32_e64 v112, v111, v107, s[54:55]
	v_cndmask_b32_e64 v111, v114, v106, s[54:55]
	v_cndmask_b32_e64 v113, v113, v158, s[54:55]
	v_mov_b32_e32 v114, v112
	v_mov_b32_e32 v115, v111
	v_mov_b32_e32 v117, v113
	v_mov_b32_dpp v114, v114 quad_perm:[1,0,3,2] row_mask:0xf bank_mask:0xf
	v_mov_b32_dpp v115, v115 quad_perm:[1,0,3,2] row_mask:0xf bank_mask:0xf
	v_mov_b32_dpp v117, v117 quad_perm:[1,0,3,2] row_mask:0xf bank_mask:0xf
	v_cmp_gt_f32_e64 s[56:57], v114, v112
	v_cmp_eq_f32_e64 s[30:31], v114, v112
	v_cmp_lt_i32_e64 s[58:59], v117, v113
	s_and_b64 s[30:31], s[30:31], s[58:59]
	s_or_b64 s[56:57], s[56:57], s[30:31]
.LBB0_1340:
	v_cndmask_b32_e64 v112, v112, v114, s[56:57]
	v_cndmask_b32_e64 v113, v113, v117, s[56:57]
	v_cndmask_b32_e64 v114, v111, v115, s[56:57]
	v_mov_b32_e32 v111, v112
	v_mov_b32_e32 v115, v114
	v_mov_b32_e32 v117, v113
	v_mov_b32_dpp v111, v111 quad_perm:[2,3,0,1] row_mask:0xf bank_mask:0xf
	v_mov_b32_dpp v115, v115 quad_perm:[2,3,0,1] row_mask:0xf bank_mask:0xf
	v_mov_b32_dpp v117, v117 quad_perm:[2,3,0,1] row_mask:0xf bank_mask:0xf
	v_cmp_gt_f32_e64 s[24:25], v111, v112
	v_cmp_eq_f32_e64 s[30:31], v111, v112
	v_cmp_lt_i32_e64 s[56:57], v117, v113
	s_and_b64 s[30:31], s[30:31], s[56:57]
	s_or_b64 s[24:25], s[24:25], s[30:31]
.LBB0_1344:
	v_cndmask_b32_e64 v111, v112, v111, s[24:25]
	v_cndmask_b32_e64 v112, v113, v117, s[24:25]
	v_cndmask_b32_e64 v113, v114, v115, s[24:25]
	v_mov_b32_e32 v114, v111
	v_mov_b32_e32 v115, v113
	v_mov_b32_e32 v117, v112
	v_mov_b32_dpp v114, v114 row_half_mirror row_mask:0xf bank_mask:0xf
	v_mov_b32_dpp v115, v115 row_half_mirror row_mask:0xf bank_mask:0xf
	v_mov_b32_dpp v117, v117 row_half_mirror row_mask:0xf bank_mask:0xf
	v_cmp_nlt_f32_e64 s[54:55], v111, v114
	s_mov_b64 s[56:57], -1
	s_mov_b64 s[30:31], -1
	s_and_saveexec_b64 s[24:25], s[54:55]
	s_cbranch_execz .LBB0_1348
	v_cmp_eq_f32_e64 s[54:55], v111, v114
	s_mov_b64 s[30:31], 0
	s_and_saveexec_b64 s[58:59], s[54:55]
	v_cmp_lt_i32_e64 s[54:55], v117, v112
	s_and_b64 s[30:31], s[54:55], exec
	s_or_b64 exec, exec, s[58:59]
	s_orn2_b64 s[30:31], s[30:31], exec
; template <int CTRL> __device__ __forceinline__ void topk_step(float& bk, int& be, float& bs) {
;     const float ok = dppf<CTRL>(bk, bk), os = dppf<CTRL>(bs, bs); const int oe = __builtin_amdgcn_update_dpp(be, be, CTRL, 0xf, 0xf, false); topk_better(bk, be, bs, ok, oe, os); }
; __device__ __forceinline__ void ph_ln_router(const Frame& F, int l, bool dry = false) {
;     ...
;             for (int sel = 0; sel < 6; ++sel) {
;                 float bk = -1e30f, bs = 0.f; int be = 0;
; #pragma unroll
;                 for (int q = 0; q < 4; ++q) if (!((taken >> q) & 1u) && key[q] > bk) { bk = key[q]; be = tk + 16 * q; bs = sc[q]; }
;                 topk_step<0xB1>(bk, be, bs); topk_step<0x4E>(bk, be, bs); topk_step<0x141>(bk, be, bs); topk_step<0x140>(bk, be, bs);
;                 if ((be & 15) == tk) taken |= 1u << (be >> 4);
;                 se[sel] = be; ss[sel] = bs; tot += bs;
.LBB0_1348:
	s_or_b64 exec, exec, s[24:25]
	v_cndmask_b32_e64 v118, v111, v114, s[30:31]
	v_cndmask_b32_e64 v114, v112, v117, s[30:31]
	v_cndmask_b32_e64 v111, v113, v115, s[30:31]
	v_mov_b32_e32 v115, v118
	v_mov_b32_e32 v112, v111
	v_mov_b32_e32 v113, v114
	v_mov_b32_dpp v115, v115 row_mirror row_mask:0xf bank_mask:0xf
	v_mov_b32_dpp v112, v112 row_mirror row_mask:0xf bank_mask:0xf
	v_mov_b32_dpp v113, v113 row_mirror row_mask:0xf bank_mask:0xf
	v_cmp_gt_f32_e64 s[56:57], v115, v118
	v_cmp_eq_f32_e64 s[24:25], v115, v118
	v_cmp_lt_i32_e64 s[30:31], v113, v114
	s_and_b64 s[24:25], s[24:25], s[30:31]
	s_or_b64 s[56:57], s[56:57], s[24:25]
.LBB0_1352:
	v_cndmask_b32_e64 v113, v114, v113, s[56:57]
	v_and_b32_e32 v114, 15, v113
	v_ashrrev_i32_e32 v115, 4, v113
	v_lshlrev_b32_e64 v115, v115, 1
	v_cmp_eq_u32_e64 s[54:55], v114, v1
	s_mov_b64 s[24:25], -1
	s_nop 0
	v_cndmask_b32_e64 v117, 0, v115, s[54:55]
	v_bitop3_b32 v114, v117, 1, v116 bitop3:0xc8
	v_cmp_eq_u32_e64 s[54:55], 0, v114
	s_and_b64 s[54:55], vcc, s[54:55]
	v_bitop3_b32 v119, v117, 2, v116 bitop3:0xc8
	v_cndmask_b32_e64 v114, v188, v101, s[54:55]
	v_cndmask_b32_e64 v115, 0, v100, s[54:55]
	v_cndmask_b32_e64 v118, 0, v1, s[54:55]
	v_cmp_eq_u32_e64 s[54:55], 0, v119
	v_cmp_gt_f32_e64 s[58:59], v103, v114
	s_and_b64 s[54:55], s[54:55], s[58:59]
	v_cndmask_b32_e64 v114, v114, v103, s[54:55]
	v_bitop3_b32 v119, v117, 4, v116 bitop3:0xc8
	v_cndmask_b32_e64 v115, v115, v102, s[54:55]
	v_cndmask_b32_e64 v118, v118, v156, s[54:55]
	v_cmp_eq_u32_e64 s[54:55], 0, v119
	v_cmp_gt_f32_e64 s[58:59], v105, v114
	s_and_b64 s[54:55], s[54:55], s[58:59]
	v_cndmask_b32_e64 v114, v114, v105, s[54:55]
	v_cndmask_b32_e64 v119, v115, v104, s[54:55]
	v_bitop3_b32 v115, v117, 8, v116 bitop3:0xc8
	v_cndmask_b32_e64 v118, v118, v157, s[54:55]
	v_cmp_eq_u32_e64 s[54:55], 0, v115
	v_cmp_gt_f32_e64 s[58:59], v107, v114
	s_and_b64 s[54:55], s[54:55], s[58:59]
	v_cndmask_b32_e64 v115, v114, v107, s[54:55]
	v_cndmask_b32_e64 v114, v119, v106, s[54:55]
	v_cndmask_b32_e64 v118, v118, v158, s[54:55]
	v_mov_b32_e32 v119, v115
	v_mov_b32_e32 v120, v114
	v_mov_b32_e32 v121, v118
	v_mov_b32_dpp v119, v119 quad_perm:[1,0,3,2] row_mask:0xf bank_mask:0xf
	v_mov_b32_dpp v120, v120 quad_perm:[1,0,3,2] row_mask:0xf bank_mask:0xf
	v_mov_b32_dpp v121, v121 quad_perm:[1,0,3,2] row_mask:0xf bank_mask:0xf
	v_cmp_nlt_f32_e64 s[54:55], v115, v119
	s_mov_b64 s[58:59], -1
	s_and_saveexec_b64 s[30:31], s[54:55]
	s_cbranch_execz .LBB0_1356
	v_cmp_eq_f32_e64 s[54:55], v115, v119
	s_mov_b64 s[58:59], 0
	s_and_saveexec_b64 s[84:85], s[54:55]
	v_cmp_lt_i32_e64 s[54:55], v121, v118
	s_and_b64 s[58:59], s[54:55], exec
	s_or_b64 exec, exec, s[84:85]
	s_orn2_b64 s[58:59], s[58:59], exec
.LBB0_1356:
	s_or_b64 exec, exec, s[30:31]
	v_cndmask_b32_e64 v115, v115, v119, s[58:59]
	v_cndmask_b32_e64 v118, v118, v121, s[58:59]
	v_cndmask_b32_e64 v119, v114, v120, s[58:59]
	v_mov_b32_e32 v114, v115
	v_mov_b32_e32 v120, v119
	v_mov_b32_e32 v121, v118
	v_mov_b32_dpp v114, v114 quad_perm:[2,3,0,1] row_mask:0xf bank_mask:0xf
	v_mov_b32_dpp v120, v120 quad_perm:[2,3,0,1] row_mask:0xf bank_mask:0xf
	v_mov_b32_dpp v121, v121 quad_perm:[2,3,0,1] row_mask:0xf bank_mask:0xf
	v_cmp_gt_f32_e64 s[24:25], v114, v115
	v_cmp_eq_f32_e64 s[30:31], v114, v115
	v_cmp_lt_i32_e64 s[58:59], v121, v118
	s_and_b64 s[30:31], s[30:31], s[58:59]
	s_or_b64 s[24:25], s[24:25], s[30:31]
.LBB0_1360:
	v_cndmask_b32_e64 v114, v115, v114, s[24:25]
	v_cndmask_b32_e64 v115, v118, v121, s[24:25]
	v_cndmask_b32_e64 v118, v119, v120, s[24:25]
	v_mov_b32_e32 v119, v114
	v_mov_b32_e32 v121, v118
	v_mov_b32_e32 v120, v115
	v_mov_b32_dpp v119, v119 row_half_mirror row_mask:0xf bank_mask:0xf
	v_mov_b32_dpp v121, v121 row_half_mirror row_mask:0xf bank_mask:0xf
	v_mov_b32_dpp v120, v120 row_half_mirror row_mask:0xf bank_mask:0xf
	v_cmp_nlt_f32_e64 s[54:55], v114, v119
	s_mov_b64 s[84:85], -1
	s_mov_b64 s[30:31], -1
	s_and_saveexec_b64 s[24:25], s[54:55]
	s_cbranch_execz .LBB0_1364
	v_cmp_eq_f32_e64 s[54:55], v114, v119
	s_mov_b64 s[30:31], 0
	s_and_saveexec_b64 s[58:59], s[54:55]
	v_cmp_lt_i32_e64 s[54:55], v120, v115
	s_and_b64 s[30:31], s[54:55], exec
	s_or_b64 exec, exec, s[58:59]
	s_orn2_b64 s[30:31], s[30:31], exec
.LBB0_1364:
	s_or_b64 exec, exec, s[24:25]
	v_cndmask_b32_e64 v119, v114, v119, s[30:31]
	v_cndmask_b32_e64 v120, v115, v120, s[30:31]
	v_cndmask_b32_e64 v114, v118, v121, s[30:31]
	v_mov_b32_e32 v121, v119
	v_mov_b32_e32 v115, v114
	v_mov_b32_e32 v118, v120
	v_mov_b32_dpp v121, v121 row_mirror row_mask:0xf bank_mask:0xf
	v_mov_b32_dpp v115, v115 row_mirror row_mask:0xf bank_mask:0xf
	v_mov_b32_dpp v118, v118 row_mirror row_mask:0xf bank_mask:0xf
	v_cmp_gt_f32_e64 s[84:85], v121, v119
	v_cmp_eq_f32_e64 s[24:25], v121, v119
	v_cmp_lt_i32_e64 s[58:59], v118, v120
	s_and_b64 s[24:25], s[24:25], s[58:59]
	s_or_b64 s[84:85], s[84:85], s[24:25]
; template <int CTRL> __device__ __forceinline__ void topk_step(float& bk, int& be, float& bs) {
;     const float ok = dppf<CTRL>(bk, bk), os = dppf<CTRL>(bs, bs); const int oe = __builtin_amdgcn_update_dpp(be, be, CTRL, 0xf, 0xf, false); topk_better(bk, be, bs, ok, oe, os); }
; __device__ __forceinline__ void ph_ln_router(const Frame& F, int l, bool dry = false) {
;     ...
;             for (int sel = 0; sel < 6; ++sel) {
;                 float bk = -1e30f, bs = 0.f; int be = 0;
; #pragma unroll
;                 for (int q = 0; q < 4; ++q) if (!((taken >> q) & 1u) && key[q] > bk) { bk = key[q]; be = tk + 16 * q; bs = sc[q]; }
;                 topk_step<0xB1>(bk, be, bs); topk_step<0x4E>(bk, be, bs); topk_step<0x141>(bk, be, bs); topk_step<0x140>(bk, be, bs);
;                 if ((be & 15) == tk) taken |= 1u << (be >> 4);
;                 se[sel] = be; ss[sel] = bs; tot += bs;
.LBB0_1368:
	v_or_b32_e32 v119, v117, v116
	v_cndmask_b32_e64 v116, v120, v118, s[84:85]
	v_and_b32_e32 v117, 15, v116
	v_ashrrev_i32_e32 v118, 4, v116
	v_lshlrev_b32_e64 v118, v118, 1
	v_cmp_eq_u32_e64 s[54:55], v117, v1
	s_mov_b64 s[24:25], -1
	s_nop 0
	v_cndmask_b32_e64 v120, 0, v118, s[54:55]
	v_bitop3_b32 v117, v120, 1, v119 bitop3:0xc8
	v_cmp_eq_u32_e64 s[54:55], 0, v117
	s_and_b64 s[54:55], vcc, s[54:55]
	v_bitop3_b32 v122, v120, 2, v119 bitop3:0xc8
	v_cndmask_b32_e64 v117, v188, v101, s[54:55]
	v_cndmask_b32_e64 v118, 0, v100, s[54:55]
	v_cndmask_b32_e64 v121, 0, v1, s[54:55]
	v_cmp_eq_u32_e64 s[54:55], 0, v122
	v_cmp_gt_f32_e64 s[58:59], v103, v117
	s_and_b64 s[54:55], s[54:55], s[58:59]
	v_cndmask_b32_e64 v117, v117, v103, s[54:55]
	v_bitop3_b32 v122, v120, 4, v119 bitop3:0xc8
	v_cndmask_b32_e64 v118, v118, v102, s[54:55]
	v_cndmask_b32_e64 v121, v121, v156, s[54:55]
	v_cmp_eq_u32_e64 s[54:55], 0, v122
	v_cmp_gt_f32_e64 s[58:59], v105, v117
	s_and_b64 s[54:55], s[54:55], s[58:59]
	v_cndmask_b32_e64 v117, v117, v105, s[54:55]
	v_cndmask_b32_e64 v122, v118, v104, s[54:55]
	v_bitop3_b32 v118, v120, 8, v119 bitop3:0xc8
	v_cndmask_b32_e64 v121, v121, v157, s[54:55]
	v_cmp_eq_u32_e64 s[54:55], 0, v118
	v_cmp_gt_f32_e64 s[58:59], v107, v117
	s_and_b64 s[54:55], s[54:55], s[58:59]
	v_cndmask_b32_e64 v118, v117, v107, s[54:55]
	v_cndmask_b32_e64 v117, v122, v106, s[54:55]
	v_cndmask_b32_e64 v121, v121, v158, s[54:55]
	v_mov_b32_e32 v122, v118
	v_mov_b32_e32 v123, v117
	v_mov_b32_e32 v124, v121
	v_mov_b32_dpp v122, v122 quad_perm:[1,0,3,2] row_mask:0xf bank_mask:0xf
	v_mov_b32_dpp v123, v123 quad_perm:[1,0,3,2] row_mask:0xf bank_mask:0xf
	v_mov_b32_dpp v124, v124 quad_perm:[1,0,3,2] row_mask:0xf bank_mask:0xf
	v_cmp_nlt_f32_e64 s[54:55], v118, v122
	s_mov_b64 s[58:59], -1
	s_and_saveexec_b64 s[30:31], s[54:55]
	s_cbranch_execz .LBB0_1372
	v_cmp_eq_f32_e64 s[54:55], v118, v122
	s_mov_b64 s[58:59], 0
	s_and_saveexec_b64 s[86:87], s[54:55]
	v_cmp_lt_i32_e64 s[54:55], v124, v121
	s_and_b64 s[58:59], s[54:55], exec
	s_or_b64 exec, exec, s[86:87]
	s_orn2_b64 s[58:59], s[58:59], exec
.LBB0_1372:
	s_or_b64 exec, exec, s[30:31]
	v_cndmask_b32_e64 v118, v118, v122, s[58:59]
	v_cndmask_b32_e64 v121, v121, v124, s[58:59]
	v_cndmask_b32_e64 v122, v117, v123, s[58:59]
	v_mov_b32_e32 v117, v118
	v_mov_b32_e32 v123, v122
	v_mov_b32_e32 v124, v121
	v_mov_b32_dpp v117, v117 quad_perm:[2,3,0,1] row_mask:0xf bank_mask:0xf
	v_mov_b32_dpp v123, v123 quad_perm:[2,3,0,1] row_mask:0xf bank_mask:0xf
	v_mov_b32_dpp v124, v124 quad_perm:[2,3,0,1] row_mask:0xf bank_mask:0xf
	v_cmp_gt_f32_e64 s[24:25], v117, v118
	v_cmp_eq_f32_e64 s[30:31], v117, v118
	v_cmp_lt_i32_e64 s[58:59], v124, v121
	s_and_b64 s[30:31], s[30:31], s[58:59]
	s_or_b64 s[24:25], s[24:25], s[30:31]
.LBB0_1376:
	v_cndmask_b32_e64 v117, v118, v117, s[24:25]
	v_cndmask_b32_e64 v118, v121, v124, s[24:25]
	v_cndmask_b32_e64 v121, v122, v123, s[24:25]
	v_mov_b32_e32 v122, v117
	v_mov_b32_e32 v124, v121
	v_mov_b32_e32 v123, v118
	v_mov_b32_dpp v122, v122 row_half_mirror row_mask:0xf bank_mask:0xf
	v_mov_b32_dpp v124, v124 row_half_mirror row_mask:0xf bank_mask:0xf
	v_mov_b32_dpp v123, v123 row_half_mirror row_mask:0xf bank_mask:0xf
	v_cmp_nlt_f32_e64 s[54:55], v117, v122
	s_mov_b64 s[24:25], -1
	s_mov_b64 s[58:59], -1
	s_and_saveexec_b64 s[30:31], s[54:55]
	s_cbranch_execz .LBB0_1380
	v_cmp_eq_f32_e64 s[54:55], v117, v122
	s_mov_b64 s[58:59], 0
	s_and_saveexec_b64 s[86:87], s[54:55]
	v_cmp_lt_i32_e64 s[54:55], v123, v118
	s_and_b64 s[58:59], s[54:55], exec
	s_or_b64 exec, exec, s[86:87]
	s_orn2_b64 s[58:59], s[58:59], exec
.LBB0_1380:
	s_or_b64 exec, exec, s[30:31]
	v_cndmask_b32_e64 v122, v117, v122, s[58:59]
	v_cndmask_b32_e64 v123, v118, v123, s[58:59]
	v_cndmask_b32_e64 v117, v121, v124, s[58:59]
	v_mov_b32_e32 v124, v122
	v_mov_b32_e32 v118, v117
	v_mov_b32_e32 v121, v123
	v_mov_b32_dpp v124, v124 row_mirror row_mask:0xf bank_mask:0xf
	v_mov_b32_dpp v118, v118 row_mirror row_mask:0xf bank_mask:0xf
	v_mov_b32_dpp v121, v121 row_mirror row_mask:0xf bank_mask:0xf
	v_cmp_gt_f32_e64 s[24:25], v124, v122
	v_cmp_eq_f32_e64 s[30:31], v124, v122
	v_cmp_lt_i32_e64 s[58:59], v121, v123
	s_and_b64 s[30:31], s[30:31], s[58:59]
	s_or_b64 s[24:25], s[24:25], s[30:31]
.LBB0_1384:
	v_or_b32_e32 v122, v120, v119
	v_cndmask_b32_e64 v119, v123, v121, s[24:25]
	v_and_b32_e32 v120, 15, v119
	v_ashrrev_i32_e32 v121, 4, v119
	v_lshlrev_b32_e64 v121, v121, 1
	v_cmp_eq_u32_e64 s[54:55], v120, v1
	s_mov_b64 s[30:31], -1
	s_mov_b64 s[86:87], -1
	v_cndmask_b32_e64 v123, 0, v121, s[54:55]
	v_bitop3_b32 v120, v123, 1, v122 bitop3:0xc8
	v_cmp_eq_u32_e64 s[54:55], 0, v120
	s_and_b64 s[54:55], vcc, s[54:55]
	v_bitop3_b32 v125, v123, 2, v122 bitop3:0xc8
	v_cndmask_b32_e64 v120, v188, v101, s[54:55]
	v_cndmask_b32_e64 v121, 0, v100, s[54:55]
	v_cndmask_b32_e64 v124, 0, v1, s[54:55]
	v_cmp_eq_u32_e64 s[54:55], 0, v125
	v_cmp_gt_f32_e64 s[58:59], v103, v120
	s_and_b64 s[54:55], s[54:55], s[58:59]
	v_cndmask_b32_e64 v120, v120, v103, s[54:55]
	v_bitop3_b32 v125, v123, 4, v122 bitop3:0xc8
	v_cndmask_b32_e64 v121, v121, v102, s[54:55]
	v_cndmask_b32_e64 v124, v124, v156, s[54:55]
	v_cmp_eq_u32_e64 s[54:55], 0, v125
	v_cmp_gt_f32_e64 s[58:59], v105, v120
	s_and_b64 s[54:55], s[54:55], s[58:59]
	v_cndmask_b32_e64 v120, v120, v105, s[54:55]
	v_cndmask_b32_e64 v125, v121, v104, s[54:55]
	v_bitop3_b32 v121, v123, 8, v122 bitop3:0xc8
	v_cndmask_b32_e64 v124, v124, v157, s[54:55]
	v_cmp_eq_u32_e64 s[54:55], 0, v121
	v_cmp_gt_f32_e64 s[58:59], v107, v120
	s_and_b64 s[54:55], s[54:55], s[58:59]
	v_cndmask_b32_e64 v121, v120, v107, s[54:55]
	v_cndmask_b32_e64 v120, v125, v106, s[54:55]
	v_cndmask_b32_e64 v124, v124, v158, s[54:55]
	v_mov_b32_e32 v125, v121
	v_mov_b32_e32 v126, v120
	v_mov_b32_e32 v127, v124
	v_mov_b32_dpp v125, v125 quad_perm:[1,0,3,2] row_mask:0xf bank_mask:0xf
	v_mov_b32_dpp v126, v126 quad_perm:[1,0,3,2] row_mask:0xf bank_mask:0xf
	v_mov_b32_dpp v127, v127 quad_perm:[1,0,3,2] row_mask:0xf bank_mask:0xf
	v_cmp_gt_f32_e64 s[86:87], v125, v121
	v_cmp_eq_f32_e64 s[58:59], v125, v121
	v_cmp_lt_i32_e64 s[26:27], v127, v124
	s_and_b64 s[58:59], s[58:59], s[26:27]
	s_or_b64 s[86:87], s[86:87], s[58:59]
; template <int CTRL> __device__ __forceinline__ void topk_step(float& bk, int& be, float& bs) {
;     const float ok = dppf<CTRL>(bk, bk), os = dppf<CTRL>(bs, bs); const int oe = __builtin_amdgcn_update_dpp(be, be, CTRL, 0xf, 0xf, false); topk_better(bk, be, bs, ok, oe, os); }
; __device__ __forceinline__ void ph_ln_router(const Frame& F, int l, bool dry = false) {
;     ...
;             for (int sel = 0; sel < 6; ++sel) {
;                 float bk = -1e30f, bs = 0.f; int be = 0;
; #pragma unroll
;                 for (int q = 0; q < 4; ++q) if (!((taken >> q) & 1u) && key[q] > bk) { bk = key[q]; be = tk + 16 * q; bs = sc[q]; }
;                 topk_step<0xB1>(bk, be, bs); topk_step<0x4E>(bk, be, bs); topk_step<0x141>(bk, be, bs); topk_step<0x140>(bk, be, bs);
;                 if ((be & 15) == tk) taken |= 1u << (be >> 4);
;                 se[sel] = be; ss[sel] = bs; tot += bs;
.LBB0_1388:
	v_cndmask_b32_e64 v121, v121, v125, s[86:87]
	v_cndmask_b32_e64 v124, v124, v127, s[86:87]
	v_cndmask_b32_e64 v125, v120, v126, s[86:87]
	v_mov_b32_e32 v120, v121
	v_mov_b32_e32 v126, v125
	v_mov_b32_e32 v127, v124
	v_mov_b32_dpp v120, v120 quad_perm:[2,3,0,1] row_mask:0xf bank_mask:0xf
	v_mov_b32_dpp v126, v126 quad_perm:[2,3,0,1] row_mask:0xf bank_mask:0xf
	v_mov_b32_dpp v127, v127 quad_perm:[2,3,0,1] row_mask:0xf bank_mask:0xf
	v_cmp_gt_f32_e64 s[30:31], v120, v121
	v_cmp_eq_f32_e64 s[58:59], v120, v121
	v_cmp_lt_i32_e64 s[26:27], v127, v124
	s_and_b64 s[58:59], s[58:59], s[26:27]
	s_or_b64 s[30:31], s[30:31], s[58:59]
.LBB0_1392:
	v_cndmask_b32_e64 v120, v121, v120, s[30:31]
	v_cndmask_b32_e64 v121, v124, v127, s[30:31]
	v_cndmask_b32_e64 v124, v125, v126, s[30:31]
	v_mov_b32_e32 v125, v120
	v_mov_b32_e32 v126, v124
	v_mov_b32_e32 v127, v121
	v_mov_b32_dpp v125, v125 row_half_mirror row_mask:0xf bank_mask:0xf
	v_mov_b32_dpp v126, v126 row_half_mirror row_mask:0xf bank_mask:0xf
	v_mov_b32_dpp v127, v127 row_half_mirror row_mask:0xf bank_mask:0xf
	v_cmp_nlt_f32_e64 s[54:55], v120, v125
	s_mov_b64 s[58:59], -1
	s_mov_b64 s[86:87], -1
	s_and_saveexec_b64 s[30:31], s[54:55]
	s_cbranch_execz .LBB0_1396
	v_cmp_eq_f32_e64 s[54:55], v120, v125
	s_mov_b64 s[86:87], 0
	s_and_saveexec_b64 s[26:27], s[54:55]
	v_cmp_lt_i32_e64 s[54:55], v127, v121
	s_and_b64 s[86:87], s[54:55], exec
	s_or_b64 exec, exec, s[26:27]
	s_orn2_b64 s[86:87], s[86:87], exec
.LBB0_1396:
	s_or_b64 exec, exec, s[30:31]
	v_cndmask_b32_e64 v128, v120, v125, s[86:87]
	v_cndmask_b32_e64 v125, v121, v127, s[86:87]
	v_cndmask_b32_e64 v120, v124, v126, s[86:87]
	v_mov_b32_e32 v126, v128
	v_mov_b32_e32 v121, v120
	v_mov_b32_e32 v124, v125
	v_mov_b32_dpp v126, v126 row_mirror row_mask:0xf bank_mask:0xf
	v_mov_b32_dpp v121, v121 row_mirror row_mask:0xf bank_mask:0xf
	v_mov_b32_dpp v124, v124 row_mirror row_mask:0xf bank_mask:0xf
	v_cmp_gt_f32_e64 s[58:59], v126, v128
	v_cmp_eq_f32_e64 s[30:31], v126, v128
	v_cmp_lt_i32_e64 s[26:27], v124, v125
	s_and_b64 s[30:31], s[30:31], s[26:27]
	s_or_b64 s[58:59], s[58:59], s[30:31]
.LBB0_1400:
	v_or_b32_e32 v123, v123, v122
	v_cndmask_b32_e64 v122, v125, v124, s[58:59]
	v_and_b32_e32 v124, 15, v122
	v_ashrrev_i32_e32 v125, 4, v122
	v_lshlrev_b32_e64 v125, v125, 1
	v_cmp_eq_u32_e64 s[54:55], v124, v1
	s_mov_b64 s[30:31], -1
	s_mov_b64 s[86:87], -1
	v_cndmask_b32_e64 v124, 0, v125, s[54:55]
	v_bitop3_b32 v125, v124, 1, v123 bitop3:0xc8
	v_cmp_eq_u32_e64 s[54:55], 0, v125
	s_and_b64 vcc, vcc, s[54:55]
	v_cndmask_b32_e32 v101, v188, v101, vcc
	v_bitop3_b32 v126, v124, 2, v123 bitop3:0xc8
	v_cndmask_b32_e32 v100, 0, v100, vcc
	v_cndmask_b32_e32 v125, 0, v1, vcc
	v_cmp_eq_u32_e32 vcc, 0, v126
	v_cmp_gt_f32_e64 s[54:55], v103, v101
	s_and_b64 vcc, vcc, s[54:55]
	v_cndmask_b32_e32 v101, v101, v103, vcc
	v_bitop3_b32 v103, v124, 4, v123 bitop3:0xc8
	v_cndmask_b32_e32 v100, v100, v102, vcc
	v_cndmask_b32_e32 v102, v125, v156, vcc
	v_cmp_eq_u32_e32 vcc, 0, v103
	v_cmp_gt_f32_e64 s[54:55], v105, v101
	s_and_b64 vcc, vcc, s[54:55]
	v_cndmask_b32_e32 v101, v101, v105, vcc
	v_bitop3_b32 v103, v124, 8, v123 bitop3:0xc8
	v_cndmask_b32_e32 v100, v100, v104, vcc
	v_cndmask_b32_e32 v102, v102, v157, vcc
	v_cmp_eq_u32_e32 vcc, 0, v103
	v_cmp_gt_f32_e64 s[54:55], v107, v101
	s_and_b64 vcc, vcc, s[54:55]
	v_cndmask_b32_e32 v101, v101, v107, vcc
	v_cndmask_b32_e32 v100, v100, v106, vcc
	v_cndmask_b32_e32 v102, v102, v158, vcc
	v_mov_b32_e32 v103, v101
	v_mov_b32_e32 v104, v100
	v_mov_b32_e32 v105, v102
	v_mov_b32_dpp v103, v103 quad_perm:[1,0,3,2] row_mask:0xf bank_mask:0xf
	v_mov_b32_dpp v104, v104 quad_perm:[1,0,3,2] row_mask:0xf bank_mask:0xf
	v_mov_b32_dpp v105, v105 quad_perm:[1,0,3,2] row_mask:0xf bank_mask:0xf
	v_cmp_gt_f32_e64 s[86:87], v103, v101
	v_cmp_eq_f32_e64 s[54:55], v103, v101
	v_cmp_lt_i32_e64 s[26:27], v105, v102
	s_and_b64 s[54:55], s[54:55], s[26:27]
	s_or_b64 s[86:87], s[86:87], s[54:55]
; __device__ __forceinline__ void ph_ln_router(const Frame& F, int l, bool dry = false) {
;     ...
;             for (int sel = 0; sel < 6; ++sel) {
;                 float bk = -1e30f, bs = 0.f; int be = 0;
; #pragma unroll
;                 for (int q = 0; q < 4; ++q) if (!((taken >> q) & 1u) && key[q] > bk) { bk = key[q]; be = tk + 16 * q; bs = sc[q]; }
;                 topk_step<0xB1>(bk, be, bs); topk_step<0x4E>(bk, be, bs); topk_step<0x141>(bk, be, bs); topk_step<0x140>(bk, be, bs);
;                 if ((be & 15) == tk) taken |= 1u << (be >> 4);
;                 se[sel] = be; ss[sel] = bs; tot += bs;
;             }
;             const float sc2 = 2.5f / tot;
;             if (tk < 6 && g < 2) {
;                 int e = se[0]; float w = ss[0];
; #pragma unroll
;                 for (int q = 1; q < 6; ++q) if (tk == q) { e = se[q]; w = ss[q]; }
;                 tok_e[r2 * 8 + tk] = e; tok_w[r2 * 8 + tk] = w * sc2; if (!dry) tok_p[r2 * 8 + tk] = __hip_atomic_fetch_add(hist + e, 1, __ATOMIC_RELAXED, __HIP_MEMORY_SCOPE_WORKGROUP);
;             }
.LBB0_1404:
	v_cndmask_b32_e64 v101, v101, v103, s[86:87]
	v_cndmask_b32_e64 v102, v102, v105, s[86:87]
	v_cndmask_b32_e64 v103, v100, v104, s[86:87]
	v_mov_b32_e32 v100, v101
	v_mov_b32_e32 v104, v103
	v_mov_b32_e32 v105, v102
	v_mov_b32_dpp v100, v100 quad_perm:[2,3,0,1] row_mask:0xf bank_mask:0xf
	v_mov_b32_dpp v104, v104 quad_perm:[2,3,0,1] row_mask:0xf bank_mask:0xf
	v_mov_b32_dpp v105, v105 quad_perm:[2,3,0,1] row_mask:0xf bank_mask:0xf
	v_cmp_gt_f32_e64 s[30:31], v100, v101
	v_cmp_eq_f32_e64 s[54:55], v100, v101
	v_cmp_lt_i32_e64 s[26:27], v105, v102
	s_and_b64 s[54:55], s[54:55], s[26:27]
	s_or_b64 s[30:31], s[30:31], s[54:55]
.LBB0_1408:
	v_cndmask_b32_e64 v100, v101, v100, s[30:31]
	v_cndmask_b32_e64 v101, v102, v105, s[30:31]
	v_cndmask_b32_e64 v102, v103, v104, s[30:31]
	v_mov_b32_e32 v103, v100
	v_mov_b32_e32 v104, v102
	v_mov_b32_e32 v105, v101
	v_mov_b32_dpp v103, v103 row_half_mirror row_mask:0xf bank_mask:0xf
	v_mov_b32_dpp v104, v104 row_half_mirror row_mask:0xf bank_mask:0xf
	v_mov_b32_dpp v105, v105 row_half_mirror row_mask:0xf bank_mask:0xf
	v_cmp_nlt_f32_e32 vcc, v100, v103
	s_mov_b64 s[54:55], -1
	s_mov_b64 s[86:87], -1
	s_and_saveexec_b64 s[30:31], vcc
	s_cbranch_execz .LBB0_1412
	v_cmp_eq_f32_e32 vcc, v100, v103
	s_mov_b64 s[86:87], 0
	s_and_saveexec_b64 s[26:27], vcc
	v_cmp_lt_i32_e32 vcc, v105, v101
	s_and_b64 s[86:87], vcc, exec
	s_or_b64 exec, exec, s[26:27]
	s_orn2_b64 s[86:87], s[86:87], exec
.LBB0_1412:
	s_or_b64 exec, exec, s[30:31]
	v_cndmask_b32_e64 v106, v100, v103, s[86:87]
	v_cndmask_b32_e64 v100, v101, v105, s[86:87]
	v_cndmask_b32_e64 v102, v102, v104, s[86:87]
	v_mov_b32_e32 v104, v106
	v_mov_b32_e32 v103, v102
	v_mov_b32_e32 v101, v100
	v_mov_b32_dpp v104, v104 row_mirror row_mask:0xf bank_mask:0xf
	v_mov_b32_dpp v103, v103 row_mirror row_mask:0xf bank_mask:0xf
	v_mov_b32_dpp v101, v101 row_mirror row_mask:0xf bank_mask:0xf
	v_cmp_gt_f32_e64 s[54:55], v104, v106
	v_cmp_eq_f32_e64 s[30:31], v104, v106
	v_cmp_lt_i32_e64 s[26:27], v101, v100
	s_and_b64 s[30:31], s[30:31], s[26:27]
	s_or_b64 s[54:55], s[54:55], s[30:31]
.LBB0_1416:
	s_and_saveexec_b64 s[30:31], s[66:67]
	s_cbranch_execz .LBB0_1313
	v_cndmask_b32_e64 v104, v108, v109, s[8:9]
	v_add_f32_e32 v105, 0, v104
	v_cndmask_b32_e64 v106, v111, v112, s[56:57]
	v_add_f32_e32 v105, v105, v106
	v_cndmask_b32_e64 v107, v114, v115, s[84:85]
	v_add_f32_e32 v105, v105, v107
	v_cndmask_b32_e64 v108, v117, v118, s[24:25]
	v_add_f32_e32 v105, v105, v108
	v_cndmask_b32_e64 v109, v120, v121, s[58:59]
	v_add_f32_e32 v105, v105, v109
	v_cndmask_b32_e64 v102, v102, v103, s[54:55]
	v_add_f32_e32 v103, v105, v102
	s_mov_b32 s2, 0x40200000
	v_div_scale_f32 v105, s[8:9], v103, v103, s2
	v_rcp_f32_e32 v111, v105
	v_cndmask_b32_e64 v100, v100, v101, s[54:55]
	v_cndmask_b32_e64 v101, v110, v113, s[44:45]
	v_cndmask_b32_e64 v101, v101, v116, s[46:47]
	v_fma_f32 v112, -v105, v111, 1.0
	v_fmac_f32_e32 v111, v112, v111
	v_div_scale_f32 v112, vcc, s2, v103, s2
	v_mul_f32_e32 v114, v112, v111
	v_fma_f32 v115, -v105, v114, v112
	v_fmac_f32_e32 v114, v115, v111
	v_fma_f32 v105, -v105, v114, v112
	v_div_fmas_f32 v105, v105, v111, v114
	v_div_fixup_f32 v105, v105, v103, s2
	v_cndmask_b32_e64 v103, v104, v106, s[44:45]
	v_cndmask_b32_e64 v103, v103, v107, s[46:47]
	v_cndmask_b32_e64 v101, v101, v119, s[48:49]
	v_cndmask_b32_e64 v103, v103, v108, s[48:49]
	v_cndmask_b32_e64 v101, v101, v122, s[50:51]
	v_ashrrev_i32_e32 v147, 31, v146
	v_readlane_b32 s8, v252, 12
	v_cndmask_b32_e64 v103, v103, v109, s[50:51]
	v_cndmask_b32_e64 v104, v101, v100, s[52:53]
	v_lshlrev_b64 v[100:101], 2, v[146:147]
	v_readlane_b32 s9, v252, 13
	v_cndmask_b32_e64 v106, v103, v102, s[52:53]
	v_mul_f32_e32 v105, v106, v105
	v_lshl_add_u64 v[102:103], s[8:9], 0, v[100:101]
	v_readlane_b32 s8, v252, 14
	v_readlane_b32 s9, v252, 15
	global_store_dword v[102:103], v104, off
	s_nop 0
	v_lshl_add_u64 v[102:103], s[8:9], 0, v[100:101]
	global_store_dword v[102:103], v105, off
	v_lshl_add_u32 v102, v104, 2, 0
	v_add_u32_e32 v102, 0x20280, v102
	ds_add_rtn_u32 v102, v102, v174
	v_lshl_add_u64 v[100:101], s[70:71], 0, v[100:101]
	s_waitcnt lgkmcnt(0)
	global_store_dword v[100:101], v102, off
	s_branch .LBB0_1313
